# attn: no static s_setprio raise for waves 4-7
# speedup vs baseline: 1.0255x; 1.0157x over previous
_Z11attn_kernelPKDF16_S0_PKfS2_S2_S2_S2_PfPDF16_S3_:
	s_load_dwordx8 s[4:11], s[0:1], 0x10
	v_and_b32_e32 v98, 63, v0
	v_lshlrev_b32_e32 v1, 2, v98
	s_lshr_b32 s3, s2, 4
	v_lshrrev_b32_e32 v2, 1, v0
	s_waitcnt lgkmcnt(0)
	global_load_dword v3, v1, s[4:5]
	global_load_dword v10, v1, s[6:7]
	global_load_dword v11, v1, s[8:9]
	global_load_dword v12, v1, s[10:11]
	s_load_dwordx2 s[4:5], s[0:1], 0x0
	s_lshl_b32 s6, s2, 1
	v_and_b32_e32 v1, 31, v0
	s_bfe_u32 s19, s2, 0x10003
	v_and_b32_e32 v183, 0x60, v2
	s_and_b32 s6, s6, 14
	s_lshl_b32 s16, s3, 7
	v_mov_b32_e32 v63, 0
	v_bfe_u32 v182, v0, 5, 1
	s_or_b32 s21, s6, s19
	v_or3_b32 v4, s16, v183, v1
	v_mov_b32_e32 v5, v63
	v_lshlrev_b32_e32 v62, 4, v182
	v_lshl_add_u32 v4, s21, 13, v4
	v_lshlrev_b64 v[6:7], 7, v[4:5]
	s_waitcnt lgkmcnt(0)
	v_lshl_add_u64 v[8:9], s[4:5], 0, v[62:63]
	v_add_u32_e32 v62, 0x1000, v4
	v_lshl_add_u64 v[4:5], v[8:9], 0, v[6:7]
	v_lshlrev_b64 v[6:7], 7, v[62:63]
	global_load_dwordx4 v[114:117], v[4:5], off
	global_load_dwordx4 v[118:121], v[4:5], off offset:32
	global_load_dwordx4 v[122:125], v[4:5], off offset:64
	global_load_dwordx4 v[126:129], v[4:5], off offset:96
	v_lshl_add_u64 v[4:5], v[8:9], 0, v[6:7]
	global_load_dwordx4 v[130:133], v[4:5], off
	global_load_dwordx4 v[134:137], v[4:5], off offset:32
	global_load_dwordx4 v[138:141], v[4:5], off offset:64
	global_load_dwordx4 v[142:145], v[4:5], off offset:96
	v_mbcnt_lo_u32_b32 v4, -1, 0
	v_mbcnt_hi_u32_b32 v4, -1, v4
	v_and_b32_e32 v5, 64, v4
	v_xor_b32_e32 v6, 32, v4
	v_add_u32_e32 v5, 64, v5
	v_cmp_lt_i32_e32 vcc, v6, v5
	v_xor_b32_e32 v7, 16, v4
	v_xor_b32_e32 v8, 8, v4
	v_cndmask_b32_e32 v6, v4, v6, vcc
	v_lshlrev_b32_e32 v69, 2, v6
	v_cmp_lt_i32_e32 vcc, v7, v5
	v_xor_b32_e32 v9, 4, v4
	v_xor_b32_e32 v13, 2, v4
	v_cndmask_b32_e32 v7, v4, v7, vcc
	v_lshlrev_b32_e32 v7, 2, v7
	v_cmp_lt_i32_e32 vcc, v8, v5
	v_xor_b32_e32 v14, 1, v4
	s_load_dwordx2 s[10:11], s[0:1], 0x48
	s_load_dwordx2 s[8:9], s[0:1], 0x30
	v_cndmask_b32_e32 v8, v4, v8, vcc
	v_lshlrev_b32_e32 v8, 2, v8
	v_cmp_lt_i32_e32 vcc, v9, v5
	v_readfirstlane_b32 s6, v0
	s_mov_b32 s13, 0
	v_cndmask_b32_e32 v9, v4, v9, vcc
	v_lshlrev_b32_e32 v9, 2, v9
	v_cmp_lt_i32_e32 vcc, v13, v5
	s_cmpk_lt_i32 s6, 0x100
	v_lshlrev_b32_e32 v99, 3, v182
	s_waitcnt vmcnt(10)
	v_mul_f32_e32 v6, v3, v10
	ds_bpermute_b32 v6, v69, v6
	s_waitcnt vmcnt(8)
	v_mul_f32_e32 v15, v11, v12
	ds_bpermute_b32 v15, v69, v15
	s_waitcnt lgkmcnt(0)
	v_fmac_f32_e32 v6, v3, v10
	ds_bpermute_b32 v3, v7, v6
	v_fmac_f32_e32 v15, v11, v12
	ds_bpermute_b32 v7, v7, v15
	s_waitcnt lgkmcnt(1)
	v_add_f32_e32 v3, v6, v3
	s_waitcnt lgkmcnt(0)
	v_add_f32_e32 v6, v15, v7
	ds_bpermute_b32 v7, v8, v3
	ds_bpermute_b32 v8, v8, v6
	s_waitcnt lgkmcnt(1)
	v_add_f32_e32 v3, v3, v7
	s_waitcnt lgkmcnt(0)
	v_add_f32_e32 v6, v6, v8
	ds_bpermute_b32 v7, v9, v3
	ds_bpermute_b32 v8, v9, v6
	v_cndmask_b32_e32 v9, v4, v13, vcc
	v_lshlrev_b32_e32 v180, 2, v9
	v_cmp_lt_i32_e32 vcc, v14, v5
	s_waitcnt lgkmcnt(1)
	v_add_f32_e32 v3, v3, v7
	s_waitcnt lgkmcnt(0)
	v_add_f32_e32 v6, v6, v8
	ds_bpermute_b32 v7, v180, v3
	ds_bpermute_b32 v8, v180, v6
	v_cndmask_b32_e32 v4, v4, v14, vcc
	v_lshlrev_b32_e32 v181, 2, v4
	s_waitcnt lgkmcnt(1)
	v_add_f32_e32 v78, v3, v7
	s_waitcnt lgkmcnt(0)
	v_add_f32_e32 v79, v6, v8
	ds_bpermute_b32 v80, v181, v78
	ds_bpermute_b32 v81, v181, v79
	s_cbranch_scc1 .LBB4_2
	s_setprio 0
